# speedup vs baseline: 1.0127x; 1.0028x over previous
_Z13gather_kernelPK15HIP_vector_typeIjLj2EEPKiPK6OvfRecPKDF16_PKfPDF16_:
	s_lshr_b32 s3, s2, 2
	s_and_b32 s3, s3, 0x3ffffffe
	s_and_b32 s4, s2, 1
	s_or_b32 s3, s3, s4
	s_cmpk_gt_u32 s3, 0x186
	s_cbranch_scc1 .LBB1_156
	s_load_dwordx4 s[8:11], s[0:1], 0x0
	s_movk_i32 s4, 0x80
	s_lshl_b32 s12, s3, 4
	s_addk_i32 s12, 0x800
	v_lshrrev_b32_e32 v2, 6, v0
	v_cmp_gt_u32_e64 s[4:5], s4, v0
	v_lshlrev_b32_e32 v1, 2, v0
	v_readfirstlane_b32 s62, v2
	s_and_saveexec_b64 s[6:7], s[4:5]
	v_mov_b32_e32 v2, 0
	ds_write_b32 v1, v2 offset:10832
	s_or_b64 exec, exec, s[6:7]
	s_waitcnt lgkmcnt(0)
	s_load_dwordx4 s[36:39], s[10:11], s12 offset:0x0
	v_cmp_gt_u32_e64 s[6:7], 64, v0
	s_and_saveexec_b64 s[12:13], s[6:7]
	v_mov_b32_e32 v2, 0
	ds_write_b32 v1, v2 offset:11856
	s_or_b64 exec, exec, s[12:13]
	s_waitcnt lgkmcnt(0)
	s_min_u32 s36, s36, 0x280
	s_min_u32 s37, s37, 0x280
	s_min_u32 s38, s38, 0x280
	s_min_u32 s39, s39, 0x280
	s_addk_i32 s37, 0x280
	s_addk_i32 s38, 0x500
	s_addk_i32 s39, 0x780
	s_cmp_ge_u32 s62, 2
	s_cselect_b32 s54, s37, s36
	s_cselect_b32 s59, s39, s38
	s_mov_b32 s52, s36
	s_mov_b32 s53, s36
	s_mov_b32 s55, s37
	s_mov_b32 s56, s37
	s_mov_b32 s57, s38
	s_mov_b32 s58, s38
	s_mov_b32 s60, s39
	s_mov_b32 s61, s39
	s_mul_i32 s15, s3, 0x5000
	s_mul_hi_u32 s13, s3, 0x5000
	s_add_u32 s8, s8, s15
	s_addc_u32 s9, s9, s13
	v_lshlrev_b32_e32 v2, 3, v0
	v_mov_b32_e32 v3, 0
	v_lshl_add_u64 v[4:5], s[8:9], 0, v[2:3]
	s_movk_i32 s13, 0x1000
	s_barrier
	global_load_dwordx2 v[20:21], v2, s[8:9]
	global_load_dwordx2 v[18:19], v2, s[8:9] offset:2048
	v_add_co_u32_e32 v2, vcc, s13, v4
	s_movk_i32 s13, 0x2000
	s_nop 0
	v_addc_co_u32_e32 v3, vcc, 0, v5, vcc
	v_add_co_u32_e32 v6, vcc, s13, v4
	s_movk_i32 s13, 0x3000
	s_nop 0
	v_addc_co_u32_e32 v7, vcc, 0, v5, vcc
	v_add_co_u32_e32 v24, vcc, s13, v4
	v_or_b32_e32 v23, 0x400, v0
	s_nop 0
	v_addc_co_u32_e32 v25, vcc, 0, v5, vcc
	v_lshlrev_b32_e32 v8, 3, v23
	v_or_b32_e32 v22, 0x800, v0
	v_add_co_u32_e32 v26, vcc, 0x4000, v4
	global_load_dwordx2 v[16:17], v[2:3], off
	global_load_dwordx2 v[14:15], v[2:3], off offset:2048
	global_load_dwordx2 v[12:13], v8, s[8:9]
	global_load_dwordx2 v[10:11], v[6:7], off offset:2048
	v_lshlrev_b32_e32 v28, 3, v22
	v_addc_co_u32_e32 v27, vcc, 0, v5, vcc
	global_load_dwordx2 v[8:9], v[24:25], off
	global_load_dwordx2 v[6:7], v[24:25], off offset:2048
	global_load_dwordx2 v[4:5], v28, s[8:9]
	global_load_dwordx2 v[2:3], v[26:27], off offset:2048
	v_mov_b32_e32 v54, 1
	v_cmp_gt_i32_e32 vcc, s52, v0
	s_and_saveexec_b64 s[8:9], vcc
	s_waitcnt vmcnt(9)
	v_lshrrev_b32_e32 v33, 16, v20
	v_lshlrev_b32_e32 v53, 2, v33
	ds_add_rtn_u32 v43, v53, v54 offset:10832
	s_or_b64 exec, exec, s[8:9]
	v_or_b32_e32 v55, 0x100, v0
	v_cmp_gt_i32_e32 vcc, s53, v55
	s_and_saveexec_b64 s[8:9], vcc
	s_waitcnt vmcnt(8)
	v_lshrrev_b32_e32 v34, 16, v18
	v_lshlrev_b32_e32 v53, 2, v34
	ds_add_rtn_u32 v44, v53, v54 offset:10832
	s_or_b64 exec, exec, s[8:9]
	v_or_b32_e32 v55, 0x200, v0
	v_cmp_gt_i32_e32 vcc, s54, v55
	s_and_saveexec_b64 s[8:9], vcc
	s_waitcnt vmcnt(7)
	v_lshrrev_b32_e32 v35, 16, v16
	v_lshlrev_b32_e32 v53, 2, v35
	ds_add_rtn_u32 v45, v53, v54 offset:10832
	s_or_b64 exec, exec, s[8:9]
	v_or_b32_e32 v55, 0x300, v0
	v_cmp_gt_i32_e32 vcc, s55, v55
	s_and_saveexec_b64 s[8:9], vcc
	s_waitcnt vmcnt(6)
	v_lshrrev_b32_e32 v36, 16, v14
	v_lshlrev_b32_e32 v53, 2, v36
	ds_add_rtn_u32 v46, v53, v54 offset:10832
	s_or_b64 exec, exec, s[8:9]
	v_or_b32_e32 v55, 0x400, v0
	v_cmp_gt_i32_e32 vcc, s56, v55
	s_and_saveexec_b64 s[8:9], vcc
	s_waitcnt vmcnt(5)
	v_lshrrev_b32_e32 v37, 16, v12
	v_lshlrev_b32_e32 v53, 2, v37
	ds_add_rtn_u32 v47, v53, v54 offset:10832
	s_or_b64 exec, exec, s[8:9]
	v_or_b32_e32 v55, 0x500, v0
	v_cmp_gt_i32_e32 vcc, s57, v55
	s_and_saveexec_b64 s[8:9], vcc
	s_waitcnt vmcnt(4)
	v_lshrrev_b32_e32 v38, 16, v10
	v_lshlrev_b32_e32 v53, 2, v38
	ds_add_rtn_u32 v48, v53, v54 offset:10832
	s_or_b64 exec, exec, s[8:9]
	v_or_b32_e32 v55, 0x600, v0
	v_cmp_gt_i32_e32 vcc, s58, v55
	s_and_saveexec_b64 s[8:9], vcc
	s_waitcnt vmcnt(3)
	v_lshrrev_b32_e32 v39, 16, v8
	v_lshlrev_b32_e32 v53, 2, v39
	ds_add_rtn_u32 v49, v53, v54 offset:10832
	s_or_b64 exec, exec, s[8:9]
	v_or_b32_e32 v55, 0x700, v0
	v_cmp_gt_i32_e32 vcc, s59, v55
	s_and_saveexec_b64 s[8:9], vcc
	s_waitcnt vmcnt(2)
	v_lshrrev_b32_e32 v40, 16, v6
	v_lshlrev_b32_e32 v53, 2, v40
	ds_add_rtn_u32 v50, v53, v54 offset:10832
	s_or_b64 exec, exec, s[8:9]
	v_or_b32_e32 v55, 0x800, v0
	v_cmp_gt_i32_e32 vcc, s60, v55
	s_and_saveexec_b64 s[8:9], vcc
	s_waitcnt vmcnt(1)
	v_lshrrev_b32_e32 v41, 16, v4
	v_lshlrev_b32_e32 v53, 2, v41
	ds_add_rtn_u32 v51, v53, v54 offset:10832
	s_or_b64 exec, exec, s[8:9]
	v_or_b32_e32 v55, 0x900, v0
	v_cmp_gt_i32_e32 vcc, s61, v55
	s_and_saveexec_b64 s[8:9], vcc
	s_waitcnt vmcnt(0)
	v_lshrrev_b32_e32 v42, 16, v2
	v_lshlrev_b32_e32 v53, 2, v42
	ds_add_rtn_u32 v52, v53, v54 offset:10832
	s_or_b64 exec, exec, s[8:9]
	s_waitcnt lgkmcnt(0)
	v_cmp_gt_i32_e32 vcc, s52, v0
	v_lshl_or_b32 v56, v43, 8, v33
	s_nop 0
	v_cndmask_b32_e32 v32, -1, v56, vcc
	v_or_b32_e32 v55, 0x100, v0
	v_cmp_gt_i32_e32 vcc, s53, v55
	v_lshl_or_b32 v56, v44, 8, v34
	s_nop 0
	v_cndmask_b32_e32 v27, -1, v56, vcc
	v_or_b32_e32 v55, 0x200, v0
	v_cmp_gt_i32_e32 vcc, s54, v55
	v_lshl_or_b32 v56, v45, 8, v35
	s_nop 0
	v_cndmask_b32_e32 v31, -1, v56, vcc
	v_or_b32_e32 v55, 0x300, v0
	v_cmp_gt_i32_e32 vcc, s55, v55
	v_lshl_or_b32 v56, v46, 8, v36
	s_nop 0
	v_cndmask_b32_e32 v26, -1, v56, vcc
	v_or_b32_e32 v55, 0x400, v0
	v_cmp_gt_i32_e32 vcc, s56, v55
	v_lshl_or_b32 v56, v47, 8, v37
	s_nop 0
	v_cndmask_b32_e32 v30, -1, v56, vcc
	v_or_b32_e32 v55, 0x500, v0
	v_cmp_gt_i32_e32 vcc, s57, v55
	v_lshl_or_b32 v56, v48, 8, v38
	s_nop 0
	v_cndmask_b32_e32 v24, -1, v56, vcc
	v_or_b32_e32 v55, 0x600, v0
	v_cmp_gt_i32_e32 vcc, s58, v55
	v_lshl_or_b32 v56, v49, 8, v39
	s_nop 0
	v_cndmask_b32_e32 v29, -1, v56, vcc
	v_or_b32_e32 v55, 0x700, v0
	v_cmp_gt_i32_e32 vcc, s59, v55
	v_lshl_or_b32 v56, v50, 8, v40
	s_nop 0
	v_cndmask_b32_e32 v23, -1, v56, vcc
	v_or_b32_e32 v55, 0x800, v0
	v_cmp_gt_i32_e32 vcc, s60, v55
	v_lshl_or_b32 v56, v51, 8, v41
	s_nop 0
	v_cndmask_b32_e32 v28, -1, v56, vcc
	v_or_b32_e32 v55, 0x900, v0
	v_cmp_gt_i32_e32 vcc, s61, v55
	v_lshl_or_b32 v56, v52, 8, v42
	s_nop 0
	v_cndmask_b32_e32 v22, -1, v56, vcc
